# ping-pong + tile-a PV/QK(b) phase rebuilt as one 8-slot ring-fed MFMA stream prefetched during softmax phase
# speedup vs baseline: 1.0123x; 1.0123x over previous
.Lno_bload:
	v_add_u32_e32 v248, s14, v151
	v_add_u32_e32 v249, s14, v152
	ds_read_b64_tr_b16 v[224:225], v248
	ds_read_b64_tr_b16 v[226:227], v249 offset:768
	ds_read_b64_tr_b16 v[228:229], v248 offset:128
	ds_read_b64_tr_b16 v[230:231], v249 offset:896
	ds_read_b64_tr_b16 v[232:233], v248 offset:6144
	ds_read_b64_tr_b16 v[234:235], v249 offset:6912
	ds_read_b64_tr_b16 v[236:237], v248 offset:6272
	ds_read_b64_tr_b16 v[238:239], v249 offset:7040
	ds_read_b64_tr_b16 v[240:241], v248 offset:12288
	ds_read_b64_tr_b16 v[242:243], v249 offset:13056
	ds_read_b64_tr_b16 v[244:245], v248 offset:12416
	ds_read_b64_tr_b16 v[246:247], v249 offset:13184
	ds_read_b64_tr_b16 v[252:253], v248 offset:18432
	ds_read_b64_tr_b16 v[254:255], v249 offset:19200
	ds_read_b64_tr_b16 v[204:205], v248 offset:18560
	ds_read_b64_tr_b16 v[206:207], v249 offset:19328
	v_exp_f32_e32 v80, v80
	v_exp_f32_e32 v81, v81
	v_exp_f32_e32 v82, v82
	v_exp_f32_e32 v83, v83
	v_add_f32_e32 v146, 0, v80
	v_exp_f32_e32 v84, v84
	v_add_f32_e32 v146, v81, v146
	v_exp_f32_e32 v85, v85
	v_add_f32_e32 v146, v82, v146
	v_exp_f32_e32 v86, v86
	v_add_f32_e32 v146, v83, v146
	v_exp_f32_e32 v87, v87
	v_add_f32_e32 v146, v84, v146
	v_exp_f32_e32 v88, v88
	v_add_f32_e32 v146, v85, v146
	v_exp_f32_e32 v89, v89
	v_add_f32_e32 v146, v86, v146
	v_exp_f32_e32 v90, v90
	v_add_f32_e32 v146, v87, v146
	v_exp_f32_e32 v91, v91
	v_add_f32_e32 v146, v88, v146
	v_exp_f32_e32 v92, v92
	v_add_f32_e32 v146, v89, v146
	v_exp_f32_e32 v93, v93
	v_add_f32_e32 v146, v90, v146
	v_exp_f32_e32 v94, v94
	v_add_f32_e32 v146, v91, v146
	v_exp_f32_e32 v95, v95
	v_add_f32_e32 v146, v92, v146
	v_exp_f32_e32 v64, v64
	v_add_f32_e32 v146, v93, v146
	v_exp_f32_e32 v65, v65
	v_add_f32_e32 v146, v94, v146
	v_exp_f32_e32 v66, v66
	v_add_f32_e32 v146, v95, v146
	v_exp_f32_e32 v67, v67
	v_add_f32_e32 v146, v64, v146
	v_exp_f32_e32 v68, v68
	v_add_f32_e32 v146, v65, v146
	v_exp_f32_e32 v69, v69
	v_add_f32_e32 v146, v66, v146
	v_exp_f32_e32 v70, v70
	v_add_f32_e32 v146, v67, v146
	v_exp_f32_e32 v71, v71
	v_add_f32_e32 v146, v68, v146
	v_exp_f32_e32 v161, v72
	v_add_f32_e32 v146, v69, v146
	v_add_f32_e32 v146, v70, v146
	v_add_f32_e32 v146, v71, v146
	v_add_f32_e32 v72, v161, v146
	v_exp_f32_e32 v146, v73
	v_exp_f32_e32 v162, v74
	v_exp_f32_e32 v163, v75
	v_exp_f32_e32 v164, v76
	v_add_f32_e32 v72, v146, v72
	v_exp_f32_e32 v165, v77
	v_add_f32_e32 v72, v162, v72
	v_exp_f32_e32 v166, v78
	v_add_f32_e32 v72, v163, v72
	v_exp_f32_e32 v167, v79
	v_add_f32_e32 v72, v164, v72
	v_add_f32_e32 v72, v165, v72
	v_add_f32_e32 v72, v166, v72
	v_cvt_pk_bf16_f32 v76, v80, v81
	v_cvt_pk_bf16_f32 v77, v84, v85
	v_cvt_pk_bf16_f32 v78, v82, v83
	v_cvt_pk_bf16_f32 v79, v86, v87
	v_cvt_pk_bf16_f32 v64, v64, v65
	v_cvt_pk_bf16_f32 v65, v68, v69
	v_cvt_pk_bf16_f32 v68, v161, v146
	v_add_f32_e32 v159, v167, v72
	v_cvt_pk_bf16_f32 v72, v88, v89
	v_cvt_pk_bf16_f32 v73, v92, v93
	v_cvt_pk_bf16_f32 v74, v90, v91
	v_cvt_pk_bf16_f32 v75, v94, v95
	v_cvt_pk_bf16_f32 v66, v66, v67
	v_cvt_pk_bf16_f32 v67, v70, v71
	v_cvt_pk_bf16_f32 v71, v166, v167
	v_cvt_pk_bf16_f32 v69, v164, v165
	v_cvt_pk_bf16_f32 v70, v162, v163
	v_add_u32_e32 v166, s14, v153
	v_add_u32_e32 v167, s14, v154
	s_barrier
	s_add_i32 s14, s10, -2
	s_and_b32 s14, s14, 3
	s_mulk_i32 s14, 0x6000
	v_add_u32_e32 v146, s14, v147
	v_add_u32_e32 v161, s14, v148
	v_add_u32_e32 v144, s14, v149
	v_add_u32_e32 v168, s14, v150
	s_waitcnt lgkmcnt(14)
	v_mfma_f32_32x32x16_bf16 v[48:63], v[224:227], v[76:79], v[48:63]
	ds_read_b64_tr_b16 v[224:225], v166
	ds_read_b64_tr_b16 v[226:227], v167 offset:768
	s_waitcnt lgkmcnt(14)
	v_mfma_f32_32x32x16_bf16 v[0:15], v[228:231], v[76:79], v[0:15]
	ds_read_b64_tr_b16 v[228:229], v166 offset:128
	ds_read_b64_tr_b16 v[230:231], v167 offset:896
	s_waitcnt lgkmcnt(14)
	v_mfma_f32_32x32x16_bf16 v[48:63], v[232:235], v[72:75], v[48:63]
	ds_read_b64_tr_b16 v[232:233], v166 offset:6144
	ds_read_b64_tr_b16 v[234:235], v167 offset:6912
	s_waitcnt lgkmcnt(14)
	v_mfma_f32_32x32x16_bf16 v[0:15], v[236:239], v[72:75], v[0:15]
	ds_read_b64_tr_b16 v[236:237], v166 offset:6272
	ds_read_b64_tr_b16 v[238:239], v167 offset:7040
	s_waitcnt lgkmcnt(14)
	v_mfma_f32_32x32x16_bf16 v[48:63], v[240:243], v[64:67], v[48:63]
	ds_read_b64_tr_b16 v[240:241], v166 offset:12288
	ds_read_b64_tr_b16 v[242:243], v167 offset:13056
	s_waitcnt lgkmcnt(14)
	v_mfma_f32_32x32x16_bf16 v[0:15], v[244:247], v[64:67], v[0:15]
	ds_read_b64_tr_b16 v[244:245], v166 offset:12416
	ds_read_b64_tr_b16 v[246:247], v167 offset:13184
	s_waitcnt lgkmcnt(14)
	v_mfma_f32_32x32x16_bf16 v[48:63], v[252:255], v[68:71], v[48:63]
	ds_read_b64_tr_b16 v[252:253], v166 offset:18432
	ds_read_b64_tr_b16 v[254:255], v167 offset:19200
	s_waitcnt lgkmcnt(14)
	v_mfma_f32_32x32x16_bf16 v[0:15], v[204:207], v[68:71], v[0:15]
	ds_read_b64_tr_b16 v[204:205], v166 offset:18560
	ds_read_b64_tr_b16 v[206:207], v167 offset:19328
	s_waitcnt lgkmcnt(14)
	v_mfma_f32_32x32x16_bf16 v[32:47], v[224:227], v[76:79], v[32:47]
	ds_read_b128 v[224:227], v146
	s_waitcnt lgkmcnt(13)
	v_mfma_f32_32x32x16_bf16 v[16:31], v[228:231], v[76:79], v[16:31]
	ds_read_b128 v[228:231], v146 offset:12288
	s_waitcnt lgkmcnt(12)
	v_mfma_f32_32x32x16_bf16 v[32:47], v[232:235], v[72:75], v[32:47]
	ds_read_b128 v[232:235], v161
	s_waitcnt lgkmcnt(11)
	v_mfma_f32_32x32x16_bf16 v[16:31], v[236:239], v[72:75], v[16:31]
	ds_read_b128 v[236:239], v161 offset:12288
	s_waitcnt lgkmcnt(10)
	v_mfma_f32_32x32x16_bf16 v[32:47], v[240:243], v[64:67], v[32:47]
	ds_read_b128 v[240:243], v144
	s_waitcnt lgkmcnt(9)
	v_mfma_f32_32x32x16_bf16 v[16:31], v[244:247], v[64:67], v[16:31]
	ds_read_b128 v[244:247], v144 offset:12288
	s_waitcnt lgkmcnt(8)
	v_mfma_f32_32x32x16_bf16 v[32:47], v[252:255], v[68:71], v[32:47]
	ds_read_b128 v[252:255], v168
	s_waitcnt lgkmcnt(7)
	v_mfma_f32_32x32x16_bf16 v[16:31], v[204:207], v[68:71], v[16:31]
	ds_read_b128 v[204:207], v168 offset:12288
	s_waitcnt lgkmcnt(7)
	v_mfma_f32_32x32x16_bf16 v[80:95], v[224:227], v[112:115], 0
	ds_read_b128 v[224:227], v146 offset:128
	s_waitcnt lgkmcnt(7)
	v_mfma_f32_32x32x16_bf16 v[64:79], v[228:231], v[112:115], 0
	ds_read_b128 v[228:231], v146 offset:12416
	s_waitcnt lgkmcnt(7)
	v_mfma_f32_32x32x16_bf16 v[80:95], v[232:235], v[116:119], v[80:95]
	ds_read_b128 v[232:235], v161 offset:128
	s_waitcnt lgkmcnt(7)
	v_mfma_f32_32x32x16_bf16 v[64:79], v[236:239], v[116:119], v[64:79]
	ds_read_b128 v[236:239], v161 offset:12416
	s_waitcnt lgkmcnt(7)
	v_mfma_f32_32x32x16_bf16 v[80:95], v[240:243], v[120:123], v[80:95]
	ds_read_b128 v[240:243], v144 offset:128
	s_waitcnt lgkmcnt(7)
	v_mfma_f32_32x32x16_bf16 v[64:79], v[244:247], v[120:123], v[64:79]
	ds_read_b128 v[244:247], v144 offset:12416
	s_waitcnt lgkmcnt(7)
	v_mfma_f32_32x32x16_bf16 v[80:95], v[252:255], v[124:127], v[80:95]
	ds_read_b128 v[252:255], v168 offset:128
	s_waitcnt lgkmcnt(7)
	v_mfma_f32_32x32x16_bf16 v[64:79], v[204:207], v[124:127], v[64:79]
	ds_read_b128 v[204:207], v168 offset:12416
	s_waitcnt lgkmcnt(7)
	v_mfma_f32_32x32x16_bf16 v[80:95], v[224:227], v[96:99], v[80:95]
	ds_read_b128 v[224:227], v146 offset:256
	s_waitcnt lgkmcnt(7)
	v_mfma_f32_32x32x16_bf16 v[64:79], v[228:231], v[96:99], v[64:79]
	ds_read_b128 v[228:231], v146 offset:12544
	s_waitcnt lgkmcnt(7)
	v_mfma_f32_32x32x16_bf16 v[80:95], v[232:235], v[100:103], v[80:95]
	ds_read_b128 v[232:235], v161 offset:256
	s_waitcnt lgkmcnt(7)
	v_mfma_f32_32x32x16_bf16 v[64:79], v[236:239], v[100:103], v[64:79]
	ds_read_b128 v[236:239], v161 offset:12544
	s_waitcnt lgkmcnt(7)
	v_mfma_f32_32x32x16_bf16 v[80:95], v[240:243], v[104:107], v[80:95]
	ds_read_b128 v[240:243], v144 offset:256
	s_waitcnt lgkmcnt(7)
	v_mfma_f32_32x32x16_bf16 v[64:79], v[244:247], v[104:107], v[64:79]
	ds_read_b128 v[244:247], v144 offset:12544
	s_waitcnt lgkmcnt(7)
	v_mfma_f32_32x32x16_bf16 v[80:95], v[252:255], v[108:111], v[80:95]
	ds_read_b128 v[252:255], v168 offset:256
	s_waitcnt lgkmcnt(7)
	v_mfma_f32_32x32x16_bf16 v[64:79], v[204:207], v[108:111], v[64:79]
	ds_read_b128 v[204:207], v168 offset:12544
	s_waitcnt lgkmcnt(7)
	v_mfma_f32_32x32x16_bf16 v[80:95], v[224:227], v[128:131], v[80:95]
	s_waitcnt lgkmcnt(6)
	v_mfma_f32_32x32x16_bf16 v[64:79], v[228:231], v[128:131], v[64:79]
	s_waitcnt lgkmcnt(5)
	v_mfma_f32_32x32x16_bf16 v[80:95], v[232:235], v[132:135], v[80:95]
	s_waitcnt lgkmcnt(4)
	v_mfma_f32_32x32x16_bf16 v[64:79], v[236:239], v[132:135], v[64:79]
	s_waitcnt lgkmcnt(3)
	v_mfma_f32_32x32x16_bf16 v[80:95], v[240:243], v[136:139], v[80:95]
	s_waitcnt lgkmcnt(2)
	v_mfma_f32_32x32x16_bf16 v[64:79], v[244:247], v[136:139], v[64:79]
	s_waitcnt lgkmcnt(1)
	v_mfma_f32_32x32x16_bf16 v[80:95], v[252:255], v[140:143], v[80:95]
	s_waitcnt lgkmcnt(0)
	v_mfma_f32_32x32x16_bf16 v[64:79], v[204:207], v[140:143], v[64:79]
	s_barrier
	s_cmp_le_u32 s7, s44
	s_cbranch_scc1 .Lf_b
	v_add_u32_e32 v146, 59, v156
	v_cmp_le_i32_e64 s[16:17], 0, v146
	v_cmp_le_i32_e64 s[18:19], 32, v146
	v_cmp_le_i32_e64 vcc, 1, v146
	s_nop 4
	v_cndmask_b32_e64 v80, v199, v80, s[16:17]
	v_cmp_le_i32_e64 s[16:17], 33, v146
	v_cndmask_b32_e64 v64, v199, v64, s[18:19]
	v_cmp_le_i32_e64 s[18:19], 2, v146
	v_cndmask_b32_e64 v81, v199, v81, vcc
	v_cmp_le_i32_e64 vcc, 34, v146
	v_cndmask_b32_e64 v65, v199, v65, s[16:17]
	v_cmp_le_i32_e64 s[16:17], 3, v146
	v_cndmask_b32_e64 v82, v199, v82, s[18:19]
	v_cmp_le_i32_e64 s[18:19], 35, v146
	v_cndmask_b32_e64 v66, v199, v66, vcc
	v_cmp_le_i32_e64 vcc, 8, v146
	v_cndmask_b32_e64 v83, v199, v83, s[16:17]
	v_cmp_le_i32_e64 s[16:17], 40, v146
	v_cndmask_b32_e64 v67, v199, v67, s[18:19]
	v_cmp_le_i32_e64 s[18:19], 9, v146
	v_cndmask_b32_e64 v84, v199, v84, vcc
	v_cmp_le_i32_e64 vcc, 41, v146
	v_cndmask_b32_e64 v68, v199, v68, s[16:17]
	v_cmp_le_i32_e64 s[16:17], 10, v146
	v_cndmask_b32_e64 v85, v199, v85, s[18:19]
	v_cmp_le_i32_e64 s[18:19], 42, v146
	v_cndmask_b32_e64 v69, v199, v69, vcc
	v_cmp_le_i32_e64 vcc, 11, v146
	v_cndmask_b32_e64 v86, v199, v86, s[16:17]
	v_cmp_le_i32_e64 s[16:17], 43, v146
	v_cndmask_b32_e64 v70, v199, v70, s[18:19]
	v_cmp_le_i32_e64 s[18:19], 16, v146
	v_cndmask_b32_e64 v87, v199, v87, vcc
	v_cmp_le_i32_e64 vcc, 48, v146
	v_cndmask_b32_e64 v71, v199, v71, s[16:17]
	v_cmp_le_i32_e64 s[16:17], 17, v146
	v_cndmask_b32_e64 v88, v199, v88, s[18:19]
	v_cmp_le_i32_e64 s[18:19], 49, v146
	v_cndmask_b32_e64 v72, v199, v72, vcc
	v_cmp_le_i32_e64 vcc, 18, v146
	v_cndmask_b32_e64 v89, v199, v89, s[16:17]
	v_cmp_le_i32_e64 s[16:17], 50, v146
	v_cndmask_b32_e64 v73, v199, v73, s[18:19]
	v_cmp_le_i32_e64 s[18:19], 19, v146
	v_cndmask_b32_e64 v90, v199, v90, vcc
	v_cmp_le_i32_e64 vcc, 51, v146
	v_cndmask_b32_e64 v74, v199, v74, s[16:17]
	v_cmp_le_i32_e64 s[16:17], 24, v146
	v_cndmask_b32_e64 v91, v199, v91, s[18:19]
	v_cmp_le_i32_e64 s[18:19], 56, v146
	v_cndmask_b32_e64 v75, v199, v75, vcc
	v_cmp_le_i32_e64 vcc, 25, v146
	v_cndmask_b32_e64 v92, v199, v92, s[16:17]
	v_cmp_le_i32_e64 s[16:17], 57, v146
	v_cndmask_b32_e64 v76, v199, v76, s[18:19]
	v_cmp_le_i32_e64 s[18:19], 26, v146
	v_cndmask_b32_e64 v93, v199, v93, vcc
	v_cmp_le_i32_e64 vcc, 58, v146
	v_cndmask_b32_e64 v77, v199, v77, s[16:17]
	v_cmp_le_i32_e64 s[16:17], 27, v146
	v_cndmask_b32_e64 v94, v199, v94, s[18:19]
	v_cmp_le_i32_e64 s[18:19], 59, v146
	v_cndmask_b32_e64 v78, v199, v78, vcc
	v_cndmask_b32_e64 v95, v199, v95, s[16:17]
	v_cndmask_b32_e64 v79, v199, v79, s[18:19]
